# attention tile head de-serialised: DMA offset vectors read under the previous tile's second PV pass, next tile's HBM->LDS requests issued first after the barrier, no LDS round trip before the first MF
# baseline (speedup 1.0000x reference)
.Lfa_tile:
	s_waitcnt vmcnt(0) lgkmcnt(0)
	s_barrier
	s_and_b32 s83, s4, 1
	s_lshl_b32 s84, s83, 15
	s_lshl_b32 s83, s83, 14
	s_add_i32 s84, s84, 0x8000
	s_add_i32 s78, s4, 1
	s_cmp_lt_u32 s78, s5
	s_cbranch_scc0 .Lfa_nodma
	s_and_b32 s64, s78, 1
	s_lshl_b32 s65, s64, 15
	s_lshl_b32 s64, s64, 14
	s_add_i32 s65, s65, 0x8000
	s_add_i32 s21, s64, s20
	s_mov_b32 m0, s21
	s_nop 0
	global_load_lds_dwordx4 v212, s[28:29]
	s_add_i32 m0, s21, 0x2000
	s_nop 0
	global_load_lds_dwordx4 v213, s[28:29]
	s_add_u32 s28, s28, 0x4000
	s_addc_u32 s29, s29, 0
	s_add_i32 s21, s65, s20
	s_mov_b32 m0, s21
	s_nop 0
	global_load_lds_dwordx4 v214, s[34:35]
	s_add_i32 m0, s21, 0x2000
	s_nop 0
	global_load_lds_dwordx4 v215, s[34:35]
	s_add_i32 m0, s21, 0x4000
	s_nop 0
	global_load_lds_dwordx4 v214, s[38:39]
	s_add_i32 m0, s21, 0x6000
	s_nop 0
	global_load_lds_dwordx4 v215, s[38:39]
	s_add_u32 s34, s34, 0x4000
	s_addc_u32 s35, s35, 0
	s_add_u32 s38, s38, 0x4000
	s_addc_u32 s39, s39, 0
.Lfa_nodma:
	v_add_u32_e32 v248, s83, v208
	s_movk_i32 s82, 0
	v_xad_u32 v244, v209, s82, v248
	s_movk_i32 s82, 32
	v_xad_u32 v245, v209, s82, v248
	s_movk_i32 s82, 64
	v_xad_u32 v246, v209, s82, v248
	s_movk_i32 s82, 96
	v_xad_u32 v247, v209, s82, v248
	ds_read_b128 v[228:231], v244 offset:0
	ds_read_b128 v[232:235], v244 offset:8192
	ds_read_b128 v[236:239], v245 offset:0
	ds_read_b128 v[240:243], v245 offset:8192
	s_waitcnt lgkmcnt(2)
	v_mfma_f32_32x32x16_bf16 v[130:145], v[228:231], v[162:165], 0
	v_mfma_f32_32x32x16_bf16 v[146:161], v[232:235], v[162:165], 0
	ds_read_b128 v[228:231], v246 offset:0
	ds_read_b128 v[232:235], v246 offset:8192
	s_waitcnt lgkmcnt(2)
	v_mfma_f32_32x32x16_bf16 v[130:145], v[236:239], v[166:169], v[130:145]
	v_mfma_f32_32x32x16_bf16 v[146:161], v[240:243], v[166:169], v[146:161]
	ds_read_b128 v[236:239], v247 offset:0
	ds_read_b128 v[240:243], v247 offset:8192
	s_waitcnt lgkmcnt(2)
	v_mfma_f32_32x32x16_bf16 v[130:145], v[228:231], v[170:173], v[130:145]
	v_mfma_f32_32x32x16_bf16 v[146:161], v[232:235], v[170:173], v[146:161]
	ds_read_b128 v[228:231], v244 offset:128
	ds_read_b128 v[232:235], v244 offset:8320
	s_waitcnt lgkmcnt(2)
	v_mfma_f32_32x32x16_bf16 v[130:145], v[236:239], v[174:177], v[130:145]
	v_mfma_f32_32x32x16_bf16 v[146:161], v[240:243], v[174:177], v[146:161]
	ds_read_b128 v[236:239], v245 offset:128
	ds_read_b128 v[240:243], v245 offset:8320
	s_waitcnt lgkmcnt(2)
	v_mfma_f32_32x32x16_bf16 v[130:145], v[228:231], v[178:181], v[130:145]
	v_mfma_f32_32x32x16_bf16 v[146:161], v[232:235], v[178:181], v[146:161]
	ds_read_b128 v[228:231], v246 offset:128
	ds_read_b128 v[232:235], v246 offset:8320
	s_waitcnt lgkmcnt(2)
	v_mfma_f32_32x32x16_bf16 v[130:145], v[236:239], v[182:185], v[130:145]
	v_mfma_f32_32x32x16_bf16 v[146:161], v[240:243], v[182:185], v[146:161]
	ds_read_b128 v[236:239], v247 offset:128
	ds_read_b128 v[240:243], v247 offset:8320
	s_waitcnt lgkmcnt(2)
	v_mfma_f32_32x32x16_bf16 v[130:145], v[228:231], v[186:189], v[130:145]
	v_mfma_f32_32x32x16_bf16 v[146:161], v[232:235], v[186:189], v[146:161]
	s_waitcnt lgkmcnt(0)
	v_mfma_f32_32x32x16_bf16 v[130:145], v[236:239], v[190:193], v[130:145]
	v_mfma_f32_32x32x16_bf16 v[146:161], v[240:243], v[190:193], v[146:161]
	v_add_u32_e32 v253, s84, v210
	ds_read_b64_tr_b16 v[228:229], v253 offset:0
	ds_read_b64_tr_b16 v[230:231], v253 offset:2048
	ds_read_b64_tr_b16 v[232:233], v253 offset:4096
	ds_read_b64_tr_b16 v[234:235], v253 offset:6144
	ds_read_b64_tr_b16 v[236:237], v253 offset:512
	ds_read_b64_tr_b16 v[238:239], v253 offset:2560
	ds_read_b64_tr_b16 v[240:241], v253 offset:4608
	ds_read_b64_tr_b16 v[242:243], v253 offset:6656
	ds_read_b64_tr_b16 v[244:245], v253 offset:1024
	ds_read_b64_tr_b16 v[246:247], v253 offset:3072
	ds_read_b64_tr_b16 v[248:249], v253 offset:5120
	ds_read_b64_tr_b16 v[250:251], v253 offset:7168
	s_cmp_ge_u32 s4, s14
	s_cbranch_scc0 .Lfa_nomask
	v_mbcnt_lo_u32_b32 v206, -1, 0
	v_mbcnt_hi_u32_b32 v206, -1, v206
	v_and_b32_e32 v203, 31, v206
	v_lshrrev_b32_e32 v206, 5, v206
	v_lshlrev_b32_e32 v206, 2, v206
	v_sub_u32_e32 v203, v203, v206
	s_lshl_b32 s21, s4, 6
	s_sub_i32 s21, s24, s21
	v_add_u32_e32 v203, s21, v203
	v_mov_b32_e32 v204, 0xff800000
	v_cmp_gt_i32_e64 vcc, 0, v203
	v_cmp_gt_i32_e64 s[48:49], 32, v203
	v_cmp_gt_i32_e64 s[50:51], 1, v203
	v_cmp_gt_i32_e64 s[52:53], 33, v203
	v_cndmask_b32_e64 v130, v130, v204, vcc
	v_cndmask_b32_e64 v146, v146, v204, s[48:49]
	v_cndmask_b32_e64 v131, v131, v204, s[50:51]
	v_cndmask_b32_e64 v147, v147, v204, s[52:53]
	v_cmp_gt_i32_e64 vcc, 2, v203
	v_cmp_gt_i32_e64 s[48:49], 34, v203
	v_cmp_gt_i32_e64 s[50:51], 3, v203
	v_cmp_gt_i32_e64 s[52:53], 35, v203
	v_cndmask_b32_e64 v132, v132, v204, vcc
	v_cndmask_b32_e64 v148, v148, v204, s[48:49]
	v_cndmask_b32_e64 v133, v133, v204, s[50:51]
	v_cndmask_b32_e64 v149, v149, v204, s[52:53]
	v_cmp_gt_i32_e64 vcc, 8, v203
	v_cmp_gt_i32_e64 s[48:49], 40, v203
	v_cmp_gt_i32_e64 s[50:51], 9, v203
	v_cmp_gt_i32_e64 s[52:53], 41, v203
	v_cndmask_b32_e64 v134, v134, v204, vcc
	v_cndmask_b32_e64 v150, v150, v204, s[48:49]
	v_cndmask_b32_e64 v135, v135, v204, s[50:51]
	v_cndmask_b32_e64 v151, v151, v204, s[52:53]
	v_cmp_gt_i32_e64 vcc, 10, v203
	v_cmp_gt_i32_e64 s[48:49], 42, v203
	v_cmp_gt_i32_e64 s[50:51], 11, v203
	v_cmp_gt_i32_e64 s[52:53], 43, v203
	v_cndmask_b32_e64 v136, v136, v204, vcc
	v_cndmask_b32_e64 v152, v152, v204, s[48:49]
	v_cndmask_b32_e64 v137, v137, v204, s[50:51]
	v_cndmask_b32_e64 v153, v153, v204, s[52:53]
	v_cmp_gt_i32_e64 vcc, 16, v203
	v_cmp_gt_i32_e64 s[48:49], 48, v203
	v_cmp_gt_i32_e64 s[50:51], 17, v203
	v_cmp_gt_i32_e64 s[52:53], 49, v203
	v_cndmask_b32_e64 v138, v138, v204, vcc
	v_cndmask_b32_e64 v154, v154, v204, s[48:49]
	v_cndmask_b32_e64 v139, v139, v204, s[50:51]
	v_cndmask_b32_e64 v155, v155, v204, s[52:53]
	v_cmp_gt_i32_e64 vcc, 18, v203
	v_cmp_gt_i32_e64 s[48:49], 50, v203
	v_cmp_gt_i32_e64 s[50:51], 19, v203
	v_cmp_gt_i32_e64 s[52:53], 51, v203
	v_cndmask_b32_e64 v140, v140, v204, vcc
	v_cndmask_b32_e64 v156, v156, v204, s[48:49]
	v_cndmask_b32_e64 v141, v141, v204, s[50:51]
	v_cndmask_b32_e64 v157, v157, v204, s[52:53]
	v_cmp_gt_i32_e64 vcc, 24, v203
	v_cmp_gt_i32_e64 s[48:49], 56, v203
	v_cmp_gt_i32_e64 s[50:51], 25, v203
	v_cmp_gt_i32_e64 s[52:53], 57, v203
	v_cndmask_b32_e64 v142, v142, v204, vcc
	v_cndmask_b32_e64 v158, v158, v204, s[48:49]
	v_cndmask_b32_e64 v143, v143, v204, s[50:51]
	v_cndmask_b32_e64 v159, v159, v204, s[52:53]
	v_cmp_gt_i32_e64 vcc, 26, v203
	v_cmp_gt_i32_e64 s[48:49], 58, v203
	v_cmp_gt_i32_e64 s[50:51], 27, v203
	v_cmp_gt_i32_e64 s[52:53], 59, v203
	v_cndmask_b32_e64 v144, v144, v204, vcc
	v_cndmask_b32_e64 v160, v160, v204, s[48:49]
	v_cndmask_b32_e64 v145, v145, v204, s[50:51]
	v_cndmask_b32_e64 v161, v161, v204, s[52:53]

.Lfa_noresc_t:
	s_waitcnt lgkmcnt(8)
	v_mfma_f32_32x32x16_bf16 v[0:15], v[212:215], v[228:231], v[0:15]
	v_exp_f32_e32 v146, v146
	v_exp_f32_e32 v147, v147
	v_mfma_f32_32x32x16_bf16 v[0:15], v[216:219], v[232:235], v[0:15]
	v_exp_f32_e32 v148, v148
	v_exp_f32_e32 v149, v149
	ds_read_b64_tr_b16 v[194:195], v253 offset:1536
	ds_read_b64_tr_b16 v[196:197], v253 offset:3584
	ds_read_b64_tr_b16 v[198:199], v253 offset:5632
	ds_read_b64_tr_b16 v[200:201], v253 offset:7680
	s_waitcnt lgkmcnt(8)
	v_mfma_f32_32x32x16_bf16 v[16:31], v[212:215], v[236:239], v[16:31]
	v_exp_f32_e32 v150, v150
	v_add_f32_e32 v252, v252, v146
	v_exp_f32_e32 v151, v151
	v_mfma_f32_32x32x16_bf16 v[16:31], v[216:219], v[240:243], v[16:31]
	v_add_f32_e32 v252, v252, v147
	v_exp_f32_e32 v152, v152
	v_add_f32_e32 v252, v252, v148
	ds_read_b64_tr_b16 v[228:229], v253 offset:16384
	ds_read_b64_tr_b16 v[230:231], v253 offset:18432
	ds_read_b64_tr_b16 v[232:233], v253 offset:20480
	ds_read_b64_tr_b16 v[234:235], v253 offset:22528
	s_waitcnt lgkmcnt(8)
	v_mfma_f32_32x32x16_bf16 v[32:47], v[212:215], v[244:247], v[32:47]
	v_exp_f32_e32 v153, v153
	v_add_f32_e32 v252, v252, v149
	v_exp_f32_e32 v154, v154
	v_mfma_f32_32x32x16_bf16 v[32:47], v[216:219], v[248:251], v[32:47]
	v_add_f32_e32 v252, v252, v150
	v_exp_f32_e32 v155, v155
	v_add_f32_e32 v252, v252, v151
	ds_read_b64_tr_b16 v[236:237], v253 offset:16896
	ds_read_b64_tr_b16 v[238:239], v253 offset:18944
	ds_read_b64_tr_b16 v[240:241], v253 offset:20992
	ds_read_b64_tr_b16 v[242:243], v253 offset:23040
	s_waitcnt lgkmcnt(8)
	v_mfma_f32_32x32x16_bf16 v[48:63], v[212:215], v[194:197], v[48:63]
	v_exp_f32_e32 v156, v156
	v_add_f32_e32 v252, v252, v152
	v_exp_f32_e32 v157, v157
	v_mfma_f32_32x32x16_bf16 v[48:63], v[216:219], v[198:201], v[48:63]
	v_add_f32_e32 v252, v252, v153
	v_exp_f32_e32 v158, v158
	v_add_f32_e32 v252, v252, v154
	ds_read_b64_tr_b16 v[244:245], v253 offset:17408
	ds_read_b64_tr_b16 v[246:247], v253 offset:19456
	ds_read_b64_tr_b16 v[248:249], v253 offset:21504
	ds_read_b64_tr_b16 v[250:251], v253 offset:23552
	s_waitcnt lgkmcnt(8)
	v_mfma_f32_32x32x16_bf16 v[64:79], v[212:215], v[228:231], v[64:79]
	v_exp_f32_e32 v159, v159
	v_add_f32_e32 v252, v252, v155
	v_exp_f32_e32 v160, v160
	v_mfma_f32_32x32x16_bf16 v[64:79], v[216:219], v[232:235], v[64:79]
	v_add_f32_e32 v252, v252, v156
	v_exp_f32_e32 v161, v161
	v_add_f32_e32 v252, v252, v157
	v_add_f32_e32 v252, v252, v158
	v_add_f32_e32 v252, v252, v159
	v_add_f32_e32 v252, v252, v160
	ds_read_b64_tr_b16 v[194:195], v253 offset:17920
	ds_read_b64_tr_b16 v[196:197], v253 offset:19968
	ds_read_b64_tr_b16 v[198:199], v253 offset:22016
	ds_read_b64_tr_b16 v[200:201], v253 offset:24064
	s_waitcnt lgkmcnt(8)
	v_mfma_f32_32x32x16_bf16 v[80:95], v[212:215], v[236:239], v[80:95]
	v_add_f32_e32 v252, v252, v161
	v_mov_b32_e32 v204, v252
	s_nop 1
	v_permlane32_swap_b32_e32 v252, v204
	v_add_f32_e32 v252, v252, v204
	v_add_f32_e32 v202, v202, v252
	v_cvt_pk_bf16_f32 v220, v146, v147
	v_cvt_pk_bf16_f32 v221, v148, v149
	v_cvt_pk_bf16_f32 v222, v150, v151
	v_mfma_f32_32x32x16_bf16 v[80:95], v[216:219], v[240:243], v[80:95]
	v_cvt_pk_bf16_f32 v223, v152, v153
	v_cvt_pk_bf16_f32 v224, v154, v155
	v_cvt_pk_bf16_f32 v225, v156, v157
	v_cvt_pk_bf16_f32 v226, v158, v159
	v_cvt_pk_bf16_f32 v227, v160, v161
	s_nop 1
	v_permlane32_swap_b32_e32 v220, v222
	v_permlane32_swap_b32_e32 v221, v223
	v_permlane32_swap_b32_e32 v224, v226
	ds_read_b64_tr_b16 v[228:229], v253 offset:8192
	ds_read_b64_tr_b16 v[230:231], v253 offset:10240
	ds_read_b64_tr_b16 v[232:233], v253 offset:12288
	ds_read_b64_tr_b16 v[234:235], v253 offset:14336
	s_waitcnt lgkmcnt(8)
	v_mfma_f32_32x32x16_bf16 v[98:113], v[212:215], v[244:247], v[98:113]
	v_permlane32_swap_b32_e32 v225, v227
	v_mfma_f32_32x32x16_bf16 v[98:113], v[216:219], v[248:251], v[98:113]
	ds_read_b64_tr_b16 v[236:237], v253 offset:8704
	ds_read_b64_tr_b16 v[238:239], v253 offset:10752
	ds_read_b64_tr_b16 v[240:241], v253 offset:12800
	ds_read_b64_tr_b16 v[242:243], v253 offset:14848
	s_waitcnt lgkmcnt(8)
	v_mfma_f32_32x32x16_bf16 v[114:129], v[212:215], v[194:197], v[114:129]
	v_mfma_f32_32x32x16_bf16 v[114:129], v[216:219], v[198:201], v[114:129]
	ds_read_b64_tr_b16 v[244:245], v253 offset:9216
	ds_read_b64_tr_b16 v[246:247], v253 offset:11264
	ds_read_b64_tr_b16 v[248:249], v253 offset:13312
	ds_read_b64_tr_b16 v[250:251], v253 offset:15360
	s_nop 1
	s_waitcnt lgkmcnt(8)
	v_mfma_f32_32x32x16_bf16 v[0:15], v[220:223], v[228:231], v[0:15]
	v_mfma_f32_32x32x16_bf16 v[0:15], v[224:227], v[232:235], v[0:15]
	ds_read_b64_tr_b16 v[194:195], v253 offset:9728
	ds_read_b64_tr_b16 v[196:197], v253 offset:11776
	ds_read_b64_tr_b16 v[198:199], v253 offset:13824
	ds_read_b64_tr_b16 v[200:201], v253 offset:15872
	s_waitcnt lgkmcnt(8)
	v_mfma_f32_32x32x16_bf16 v[16:31], v[220:223], v[236:239], v[16:31]
	v_mfma_f32_32x32x16_bf16 v[16:31], v[224:227], v[240:243], v[16:31]
	ds_read_b64_tr_b16 v[228:229], v253 offset:24576
	ds_read_b64_tr_b16 v[230:231], v253 offset:26624
	ds_read_b64_tr_b16 v[232:233], v253 offset:28672
	ds_read_b64_tr_b16 v[234:235], v253 offset:30720
	s_waitcnt lgkmcnt(8)
	v_mfma_f32_32x32x16_bf16 v[32:47], v[220:223], v[244:247], v[32:47]
	v_mfma_f32_32x32x16_bf16 v[32:47], v[224:227], v[248:251], v[32:47]
	ds_read_b64_tr_b16 v[236:237], v253 offset:25088
	ds_read_b64_tr_b16 v[238:239], v253 offset:27136
	ds_read_b64_tr_b16 v[240:241], v253 offset:29184
	ds_read_b64_tr_b16 v[242:243], v253 offset:31232
	s_waitcnt lgkmcnt(8)
	v_mfma_f32_32x32x16_bf16 v[48:63], v[220:223], v[194:197], v[48:63]
	v_mfma_f32_32x32x16_bf16 v[48:63], v[224:227], v[198:201], v[48:63]
	ds_read_b64_tr_b16 v[244:245], v253 offset:25600
	ds_read_b64_tr_b16 v[246:247], v253 offset:27648
	ds_read_b64_tr_b16 v[248:249], v253 offset:29696
	ds_read_b64_tr_b16 v[250:251], v253 offset:31744
	s_waitcnt lgkmcnt(8)
	v_mfma_f32_32x32x16_bf16 v[64:79], v[220:223], v[228:231], v[64:79]
	v_mfma_f32_32x32x16_bf16 v[64:79], v[224:227], v[232:235], v[64:79]
	ds_read_b64_tr_b16 v[194:195], v253 offset:26112
	ds_read_b64_tr_b16 v[196:197], v253 offset:28160
	ds_read_b64_tr_b16 v[198:199], v253 offset:30208
	ds_read_b64_tr_b16 v[200:201], v253 offset:32256
	s_waitcnt lgkmcnt(8)
	v_mfma_f32_32x32x16_bf16 v[80:95], v[220:223], v[236:239], v[80:95]
	v_mfma_f32_32x32x16_bf16 v[80:95], v[224:227], v[240:243], v[80:95]
	s_waitcnt lgkmcnt(4)
	v_mfma_f32_32x32x16_bf16 v[98:113], v[220:223], v[244:247], v[98:113]
	v_mfma_f32_32x32x16_bf16 v[98:113], v[224:227], v[248:251], v[98:113]
	s_waitcnt lgkmcnt(0)
	v_mfma_f32_32x32x16_bf16 v[114:129], v[220:223], v[194:197], v[114:129]
	v_mfma_f32_32x32x16_bf16 v[114:129], v[224:227], v[198:201], v[114:129]
	v_mbcnt_lo_u32_b32 v216, -1, 0
	v_mbcnt_hi_u32_b32 v216, -1, v216
	s_add_i32 s21, s20, 0x1e800
	v_lshl_add_u32 v216, v216, 2, s21
	ds_read_b32 v212, v216
	ds_read_b32 v213, v216 offset:256
	ds_read_b32 v214, v216 offset:512
	ds_read_b32 v215, v216 offset:768
	s_add_i32 s4, s4, 1
	s_cmp_lt_u32 s4, s5
	s_cbranch_scc1 .Lfa_tile
	s_waitcnt lgkmcnt(0)
	s_bitcmp1_b32 s9, 0
	s_cbranch_scc1 .Lfa_epi_c1
	s_nop 7
	s_nop 7
	v_mbcnt_lo_u32_b32 v229, -1, 0
	v_mbcnt_hi_u32_b32 v229, -1, v229
	s_lshl_b32 s21, s15, 8
	s_add_i32 s21, s21, 0x18000
	v_and_b32_e32 v231, 31, v229
	v_lshl_add_u32 v230, v231, 2, s21
	v_lshrrev_b32_e32 v229, 5, v229
	v_lshl_add_u32 v232, v229, 4, s21
	ds_write_b32 v230, v202 offset:128
	s_waitcnt lgkmcnt(0)
	ds_read_b128 v[236:239], v232 offset:128
	ds_read_b128 v[240:243], v232 offset:160
	ds_read_b128 v[244:247], v232 offset:192
	ds_read_b128 v[248:251], v232 offset:224
	s_waitcnt lgkmcnt(0)
	v_rcp_f32_e32 v236, v236
	v_rcp_f32_e32 v237, v237
	v_rcp_f32_e32 v238, v238
	v_rcp_f32_e32 v239, v239
	v_rcp_f32_e32 v240, v240
	v_rcp_f32_e32 v241, v241
	v_rcp_f32_e32 v242, v242
	v_rcp_f32_e32 v243, v243
	v_rcp_f32_e32 v244, v244
	v_rcp_f32_e32 v245, v245
	v_rcp_f32_e32 v246, v246
	v_rcp_f32_e32 v247, v247
	v_rcp_f32_e32 v248, v248
	v_rcp_f32_e32 v249, v249
	v_rcp_f32_e32 v250, v250
	v_rcp_f32_e32 v251, v251
	s_nop 0
	v_mul_f32_dpp v228, v0, v236 quad_perm:[1,0,3,2] row_mask:0xf bank_mask:0xf
	v_mul_f32_e32 v0, v0, v236
	v_cvt_pk_bf16_f32 v0, v0, v228
	v_mul_f32_dpp v228, v1, v237 quad_perm:[1,0,3,2] row_mask:0xf bank_mask:0xf
	v_mul_f32_e32 v1, v1, v237
	v_cvt_pk_bf16_f32 v1, v1, v228
	v_mul_f32_dpp v228, v2, v238 quad_perm:[1,0,3,2] row_mask:0xf bank_mask:0xf
	v_mul_f32_e32 v2, v2, v238
	v_cvt_pk_bf16_f32 v2, v2, v228
	v_mul_f32_dpp v228, v3, v239 quad_perm:[1,0,3,2] row_mask:0xf bank_mask:0xf
	v_mul_f32_e32 v3, v3, v239
	v_cvt_pk_bf16_f32 v3, v3, v228
	v_mul_f32_dpp v228, v4, v240 quad_perm:[1,0,3,2] row_mask:0xf bank_mask:0xf
	v_mul_f32_e32 v4, v4, v240
	v_cvt_pk_bf16_f32 v4, v4, v228
	v_mul_f32_dpp v228, v5, v241 quad_perm:[1,0,3,2] row_mask:0xf bank_mask:0xf
	v_mul_f32_e32 v5, v5, v241
	v_cvt_pk_bf16_f32 v5, v5, v228
	v_mul_f32_dpp v228, v6, v242 quad_perm:[1,0,3,2] row_mask:0xf bank_mask:0xf
	v_mul_f32_e32 v6, v6, v242
	v_cvt_pk_bf16_f32 v6, v6, v228
	v_mul_f32_dpp v228, v7, v243 quad_perm:[1,0,3,2] row_mask:0xf bank_mask:0xf
	v_mul_f32_e32 v7, v7, v243
	v_cvt_pk_bf16_f32 v7, v7, v228
	v_mul_f32_dpp v228, v8, v244 quad_perm:[1,0,3,2] row_mask:0xf bank_mask:0xf
	v_mul_f32_e32 v8, v8, v244
	v_cvt_pk_bf16_f32 v8, v8, v228
	v_mul_f32_dpp v228, v9, v245 quad_perm:[1,0,3,2] row_mask:0xf bank_mask:0xf
	v_mul_f32_e32 v9, v9, v245
	v_cvt_pk_bf16_f32 v9, v9, v228
	v_mul_f32_dpp v228, v10, v246 quad_perm:[1,0,3,2] row_mask:0xf bank_mask:0xf
	v_mul_f32_e32 v10, v10, v246
	v_cvt_pk_bf16_f32 v10, v10, v228
	v_mul_f32_dpp v228, v11, v247 quad_perm:[1,0,3,2] row_mask:0xf bank_mask:0xf
	v_mul_f32_e32 v11, v11, v247
	v_cvt_pk_bf16_f32 v11, v11, v228
	v_mul_f32_dpp v228, v12, v248 quad_perm:[1,0,3,2] row_mask:0xf bank_mask:0xf
	v_mul_f32_e32 v12, v12, v248
	v_cvt_pk_bf16_f32 v12, v12, v228
	v_mul_f32_dpp v228, v13, v249 quad_perm:[1,0,3,2] row_mask:0xf bank_mask:0xf
	v_mul_f32_e32 v13, v13, v249
	v_cvt_pk_bf16_f32 v13, v13, v228
	v_mul_f32_dpp v228, v14, v250 quad_perm:[1,0,3,2] row_mask:0xf bank_mask:0xf
	v_mul_f32_e32 v14, v14, v250
	v_cvt_pk_bf16_f32 v14, v14, v228
	v_mul_f32_dpp v228, v15, v251 quad_perm:[1,0,3,2] row_mask:0xf bank_mask:0xf
	v_mul_f32_e32 v15, v15, v251
	v_cvt_pk_bf16_f32 v15, v15, v228
	v_mul_f32_dpp v228, v16, v236 quad_perm:[1,0,3,2] row_mask:0xf bank_mask:0xf
	v_mul_f32_e32 v16, v16, v236
	v_cvt_pk_bf16_f32 v16, v16, v228
	v_mul_f32_dpp v228, v17, v237 quad_perm:[1,0,3,2] row_mask:0xf bank_mask:0xf
	v_mul_f32_e32 v17, v17, v237
	v_cvt_pk_bf16_f32 v17, v17, v228
	v_mul_f32_dpp v228, v18, v238 quad_perm:[1,0,3,2] row_mask:0xf bank_mask:0xf
	v_mul_f32_e32 v18, v18, v238
	v_cvt_pk_bf16_f32 v18, v18, v228
	v_mul_f32_dpp v228, v19, v239 quad_perm:[1,0,3,2] row_mask:0xf bank_mask:0xf
	v_mul_f32_e32 v19, v19, v239
	v_cvt_pk_bf16_f32 v19, v19, v228
	v_mul_f32_dpp v228, v20, v240 quad_perm:[1,0,3,2] row_mask:0xf bank_mask:0xf
	v_mul_f32_e32 v20, v20, v240
	v_cvt_pk_bf16_f32 v20, v20, v228
	v_mul_f32_dpp v228, v21, v241 quad_perm:[1,0,3,2] row_mask:0xf bank_mask:0xf
	v_mul_f32_e32 v21, v21, v241
	v_cvt_pk_bf16_f32 v21, v21, v228
	v_mul_f32_dpp v228, v22, v242 quad_perm:[1,0,3,2] row_mask:0xf bank_mask:0xf
	v_mul_f32_e32 v22, v22, v242
	v_cvt_pk_bf16_f32 v22, v22, v228
	v_mul_f32_dpp v228, v23, v243 quad_perm:[1,0,3,2] row_mask:0xf bank_mask:0xf
	v_mul_f32_e32 v23, v23, v243
	v_cvt_pk_bf16_f32 v23, v23, v228
	v_mul_f32_dpp v228, v24, v244 quad_perm:[1,0,3,2] row_mask:0xf bank_mask:0xf
	v_mul_f32_e32 v24, v24, v244
	v_cvt_pk_bf16_f32 v24, v24, v228
	v_mul_f32_dpp v228, v25, v245 quad_perm:[1,0,3,2] row_mask:0xf bank_mask:0xf
	v_mul_f32_e32 v25, v25, v245
	v_cvt_pk_bf16_f32 v25, v25, v228
	v_mul_f32_dpp v228, v26, v246 quad_perm:[1,0,3,2] row_mask:0xf bank_mask:0xf
	v_mul_f32_e32 v26, v26, v246
	v_cvt_pk_bf16_f32 v26, v26, v228
	v_mul_f32_dpp v228, v27, v247 quad_perm:[1,0,3,2] row_mask:0xf bank_mask:0xf
	v_mul_f32_e32 v27, v27, v247
	v_cvt_pk_bf16_f32 v27, v27, v228
	v_mul_f32_dpp v228, v28, v248 quad_perm:[1,0,3,2] row_mask:0xf bank_mask:0xf
	v_mul_f32_e32 v28, v28, v248
	v_cvt_pk_bf16_f32 v28, v28, v228
	v_mul_f32_dpp v228, v29, v249 quad_perm:[1,0,3,2] row_mask:0xf bank_mask:0xf
	v_mul_f32_e32 v29, v29, v249
	v_cvt_pk_bf16_f32 v29, v29, v228
	v_mul_f32_dpp v228, v30, v250 quad_perm:[1,0,3,2] row_mask:0xf bank_mask:0xf
	v_mul_f32_e32 v30, v30, v250
	v_cvt_pk_bf16_f32 v30, v30, v228
	v_mul_f32_dpp v228, v31, v251 quad_perm:[1,0,3,2] row_mask:0xf bank_mask:0xf
	v_mul_f32_e32 v31, v31, v251
	v_cvt_pk_bf16_f32 v31, v31, v228
	v_mul_f32_dpp v228, v32, v236 quad_perm:[1,0,3,2] row_mask:0xf bank_mask:0xf
	v_mul_f32_e32 v32, v32, v236
	v_cvt_pk_bf16_f32 v32, v32, v228
	v_mul_f32_dpp v228, v33, v237 quad_perm:[1,0,3,2] row_mask:0xf bank_mask:0xf
	v_mul_f32_e32 v33, v33, v237
	v_cvt_pk_bf16_f32 v33, v33, v228
	v_mul_f32_dpp v228, v34, v238 quad_perm:[1,0,3,2] row_mask:0xf bank_mask:0xf
	v_mul_f32_e32 v34, v34, v238
	v_cvt_pk_bf16_f32 v34, v34, v228
	v_mul_f32_dpp v228, v35, v239 quad_perm:[1,0,3,2] row_mask:0xf bank_mask:0xf
	v_mul_f32_e32 v35, v35, v239
	v_cvt_pk_bf16_f32 v35, v35, v228
	v_mul_f32_dpp v228, v36, v240 quad_perm:[1,0,3,2] row_mask:0xf bank_mask:0xf
	v_mul_f32_e32 v36, v36, v240
	v_cvt_pk_bf16_f32 v36, v36, v228
	v_mul_f32_dpp v228, v37, v241 quad_perm:[1,0,3,2] row_mask:0xf bank_mask:0xf
	v_mul_f32_e32 v37, v37, v241
	v_cvt_pk_bf16_f32 v37, v37, v228
	v_mul_f32_dpp v228, v38, v242 quad_perm:[1,0,3,2] row_mask:0xf bank_mask:0xf
	v_mul_f32_e32 v38, v38, v242
	v_cvt_pk_bf16_f32 v38, v38, v228
	v_mul_f32_dpp v228, v39, v243 quad_perm:[1,0,3,2] row_mask:0xf bank_mask:0xf
	v_mul_f32_e32 v39, v39, v243
	v_cvt_pk_bf16_f32 v39, v39, v228
	v_mul_f32_dpp v228, v40, v244 quad_perm:[1,0,3,2] row_mask:0xf bank_mask:0xf
	v_mul_f32_e32 v40, v40, v244
	v_cvt_pk_bf16_f32 v40, v40, v228
	v_mul_f32_dpp v228, v41, v245 quad_perm:[1,0,3,2] row_mask:0xf bank_mask:0xf
	v_mul_f32_e32 v41, v41, v245
	v_cvt_pk_bf16_f32 v41, v41, v228
	v_mul_f32_dpp v228, v42, v246 quad_perm:[1,0,3,2] row_mask:0xf bank_mask:0xf
	v_mul_f32_e32 v42, v42, v246
	v_cvt_pk_bf16_f32 v42, v42, v228
	v_mul_f32_dpp v228, v43, v247 quad_perm:[1,0,3,2] row_mask:0xf bank_mask:0xf
	v_mul_f32_e32 v43, v43, v247
	v_cvt_pk_bf16_f32 v43, v43, v228
	v_mul_f32_dpp v228, v44, v248 quad_perm:[1,0,3,2] row_mask:0xf bank_mask:0xf
	v_mul_f32_e32 v44, v44, v248
	v_cvt_pk_bf16_f32 v44, v44, v228
	v_mul_f32_dpp v228, v45, v249 quad_perm:[1,0,3,2] row_mask:0xf bank_mask:0xf
	v_mul_f32_e32 v45, v45, v249
	v_cvt_pk_bf16_f32 v45, v45, v228
	v_mul_f32_dpp v228, v46, v250 quad_perm:[1,0,3,2] row_mask:0xf bank_mask:0xf
	v_mul_f32_e32 v46, v46, v250
	v_cvt_pk_bf16_f32 v46, v46, v228
	v_mul_f32_dpp v228, v47, v251 quad_perm:[1,0,3,2] row_mask:0xf bank_mask:0xf
	v_mul_f32_e32 v47, v47, v251
	v_cvt_pk_bf16_f32 v47, v47, v228
	v_mul_f32_dpp v228, v48, v236 quad_perm:[1,0,3,2] row_mask:0xf bank_mask:0xf
	v_mul_f32_e32 v48, v48, v236
	v_cvt_pk_bf16_f32 v48, v48, v228
	v_mul_f32_dpp v228, v49, v237 quad_perm:[1,0,3,2] row_mask:0xf bank_mask:0xf
	v_mul_f32_e32 v49, v49, v237
	v_cvt_pk_bf16_f32 v49, v49, v228
	v_mul_f32_dpp v228, v50, v238 quad_perm:[1,0,3,2] row_mask:0xf bank_mask:0xf
	v_mul_f32_e32 v50, v50, v238
	v_cvt_pk_bf16_f32 v50, v50, v228
	v_mul_f32_dpp v228, v51, v239 quad_perm:[1,0,3,2] row_mask:0xf bank_mask:0xf
	v_mul_f32_e32 v51, v51, v239
	v_cvt_pk_bf16_f32 v51, v51, v228
	v_mul_f32_dpp v228, v52, v240 quad_perm:[1,0,3,2] row_mask:0xf bank_mask:0xf
	v_mul_f32_e32 v52, v52, v240
	v_cvt_pk_bf16_f32 v52, v52, v228
	v_mul_f32_dpp v228, v53, v241 quad_perm:[1,0,3,2] row_mask:0xf bank_mask:0xf
	v_mul_f32_e32 v53, v53, v241
	v_cvt_pk_bf16_f32 v53, v53, v228
	v_mul_f32_dpp v228, v54, v242 quad_perm:[1,0,3,2] row_mask:0xf bank_mask:0xf
	v_mul_f32_e32 v54, v54, v242
	v_cvt_pk_bf16_f32 v54, v54, v228
	v_mul_f32_dpp v228, v55, v243 quad_perm:[1,0,3,2] row_mask:0xf bank_mask:0xf
	v_mul_f32_e32 v55, v55, v243
	v_cvt_pk_bf16_f32 v55, v55, v228
	v_mul_f32_dpp v228, v56, v244 quad_perm:[1,0,3,2] row_mask:0xf bank_mask:0xf
	v_mul_f32_e32 v56, v56, v244
	v_cvt_pk_bf16_f32 v56, v56, v228
	v_mul_f32_dpp v228, v57, v245 quad_perm:[1,0,3,2] row_mask:0xf bank_mask:0xf
	v_mul_f32_e32 v57, v57, v245
	v_cvt_pk_bf16_f32 v57, v57, v228
	v_mul_f32_dpp v228, v58, v246 quad_perm:[1,0,3,2] row_mask:0xf bank_mask:0xf
	v_mul_f32_e32 v58, v58, v246
	v_cvt_pk_bf16_f32 v58, v58, v228
	v_mul_f32_dpp v228, v59, v247 quad_perm:[1,0,3,2] row_mask:0xf bank_mask:0xf
	v_mul_f32_e32 v59, v59, v247
	v_cvt_pk_bf16_f32 v59, v59, v228
	v_mul_f32_dpp v228, v60, v248 quad_perm:[1,0,3,2] row_mask:0xf bank_mask:0xf
	v_mul_f32_e32 v60, v60, v248
	v_cvt_pk_bf16_f32 v60, v60, v228
	v_mul_f32_dpp v228, v61, v249 quad_perm:[1,0,3,2] row_mask:0xf bank_mask:0xf
	v_mul_f32_e32 v61, v61, v249
	v_cvt_pk_bf16_f32 v61, v61, v228
	v_mul_f32_dpp v228, v62, v250 quad_perm:[1,0,3,2] row_mask:0xf bank_mask:0xf
	v_mul_f32_e32 v62, v62, v250
	v_cvt_pk_bf16_f32 v62, v62, v228
	v_mul_f32_dpp v228, v63, v251 quad_perm:[1,0,3,2] row_mask:0xf bank_mask:0xf
	v_mul_f32_e32 v63, v63, v251
	v_cvt_pk_bf16_f32 v63, v63, v228
	v_mul_f32_dpp v228, v64, v236 quad_perm:[1,0,3,2] row_mask:0xf bank_mask:0xf
	v_mul_f32_e32 v64, v64, v236
	v_cvt_pk_bf16_f32 v64, v64, v228
	v_mul_f32_dpp v228, v65, v237 quad_perm:[1,0,3,2] row_mask:0xf bank_mask:0xf
	v_mul_f32_e32 v65, v65, v237
	v_cvt_pk_bf16_f32 v65, v65, v228
	v_mul_f32_dpp v228, v66, v238 quad_perm:[1,0,3,2] row_mask:0xf bank_mask:0xf
	v_mul_f32_e32 v66, v66, v238
	v_cvt_pk_bf16_f32 v66, v66, v228
	v_mul_f32_dpp v228, v67, v239 quad_perm:[1,0,3,2] row_mask:0xf bank_mask:0xf
	v_mul_f32_e32 v67, v67, v239
	v_cvt_pk_bf16_f32 v67, v67, v228
	v_mul_f32_dpp v228, v68, v240 quad_perm:[1,0,3,2] row_mask:0xf bank_mask:0xf
	v_mul_f32_e32 v68, v68, v240
	v_cvt_pk_bf16_f32 v68, v68, v228
	v_mul_f32_dpp v228, v69, v241 quad_perm:[1,0,3,2] row_mask:0xf bank_mask:0xf
	v_mul_f32_e32 v69, v69, v241
	v_cvt_pk_bf16_f32 v69, v69, v228
	v_mul_f32_dpp v228, v70, v242 quad_perm:[1,0,3,2] row_mask:0xf bank_mask:0xf
	v_mul_f32_e32 v70, v70, v242
	v_cvt_pk_bf16_f32 v70, v70, v228
	v_mul_f32_dpp v228, v71, v243 quad_perm:[1,0,3,2] row_mask:0xf bank_mask:0xf
	v_mul_f32_e32 v71, v71, v243
	v_cvt_pk_bf16_f32 v71, v71, v228
	v_mul_f32_dpp v228, v72, v244 quad_perm:[1,0,3,2] row_mask:0xf bank_mask:0xf
	v_mul_f32_e32 v72, v72, v244
	v_cvt_pk_bf16_f32 v72, v72, v228
	v_mul_f32_dpp v228, v73, v245 quad_perm:[1,0,3,2] row_mask:0xf bank_mask:0xf
	v_mul_f32_e32 v73, v73, v245
	v_cvt_pk_bf16_f32 v73, v73, v228
	v_mul_f32_dpp v228, v74, v246 quad_perm:[1,0,3,2] row_mask:0xf bank_mask:0xf
	v_mul_f32_e32 v74, v74, v246
	v_cvt_pk_bf16_f32 v74, v74, v228
	v_mul_f32_dpp v228, v75, v247 quad_perm:[1,0,3,2] row_mask:0xf bank_mask:0xf
	v_mul_f32_e32 v75, v75, v247
	v_cvt_pk_bf16_f32 v75, v75, v228
	v_mul_f32_dpp v228, v76, v248 quad_perm:[1,0,3,2] row_mask:0xf bank_mask:0xf
	v_mul_f32_e32 v76, v76, v248
	v_cvt_pk_bf16_f32 v76, v76, v228
	v_mul_f32_dpp v228, v77, v249 quad_perm:[1,0,3,2] row_mask:0xf bank_mask:0xf
	v_mul_f32_e32 v77, v77, v249
	v_cvt_pk_bf16_f32 v77, v77, v228
	v_mul_f32_dpp v228, v78, v250 quad_perm:[1,0,3,2] row_mask:0xf bank_mask:0xf
	v_mul_f32_e32 v78, v78, v250
	v_cvt_pk_bf16_f32 v78, v78, v228
	v_mul_f32_dpp v228, v79, v251 quad_perm:[1,0,3,2] row_mask:0xf bank_mask:0xf
	v_mul_f32_e32 v79, v79, v251
	v_cvt_pk_bf16_f32 v79, v79, v228
	v_mul_f32_dpp v228, v80, v236 quad_perm:[1,0,3,2] row_mask:0xf bank_mask:0xf
	v_mul_f32_e32 v80, v80, v236
	v_cvt_pk_bf16_f32 v80, v80, v228
	v_mul_f32_dpp v228, v81, v237 quad_perm:[1,0,3,2] row_mask:0xf bank_mask:0xf
	v_mul_f32_e32 v81, v81, v237
	v_cvt_pk_bf16_f32 v81, v81, v228
	v_mul_f32_dpp v228, v82, v238 quad_perm:[1,0,3,2] row_mask:0xf bank_mask:0xf
	v_mul_f32_e32 v82, v82, v238
	v_cvt_pk_bf16_f32 v82, v82, v228
	v_mul_f32_dpp v228, v83, v239 quad_perm:[1,0,3,2] row_mask:0xf bank_mask:0xf
	v_mul_f32_e32 v83, v83, v239
	v_cvt_pk_bf16_f32 v83, v83, v228
	v_mul_f32_dpp v228, v84, v240 quad_perm:[1,0,3,2] row_mask:0xf bank_mask:0xf
	v_mul_f32_e32 v84, v84, v240
	v_cvt_pk_bf16_f32 v84, v84, v228
	v_mul_f32_dpp v228, v85, v241 quad_perm:[1,0,3,2] row_mask:0xf bank_mask:0xf
	v_mul_f32_e32 v85, v85, v241
	v_cvt_pk_bf16_f32 v85, v85, v228
	v_mul_f32_dpp v228, v86, v242 quad_perm:[1,0,3,2] row_mask:0xf bank_mask:0xf
	v_mul_f32_e32 v86, v86, v242
	v_cvt_pk_bf16_f32 v86, v86, v228
	v_mul_f32_dpp v228, v87, v243 quad_perm:[1,0,3,2] row_mask:0xf bank_mask:0xf
	v_mul_f32_e32 v87, v87, v243
	v_cvt_pk_bf16_f32 v87, v87, v228
	v_mul_f32_dpp v228, v88, v244 quad_perm:[1,0,3,2] row_mask:0xf bank_mask:0xf
	v_mul_f32_e32 v88, v88, v244
	v_cvt_pk_bf16_f32 v88, v88, v228
	v_mul_f32_dpp v228, v89, v245 quad_perm:[1,0,3,2] row_mask:0xf bank_mask:0xf
	v_mul_f32_e32 v89, v89, v245
	v_cvt_pk_bf16_f32 v89, v89, v228
	v_mul_f32_dpp v228, v90, v246 quad_perm:[1,0,3,2] row_mask:0xf bank_mask:0xf
	v_mul_f32_e32 v90, v90, v246
	v_cvt_pk_bf16_f32 v90, v90, v228
	v_mul_f32_dpp v228, v91, v247 quad_perm:[1,0,3,2] row_mask:0xf bank_mask:0xf
	v_mul_f32_e32 v91, v91, v247
	v_cvt_pk_bf16_f32 v91, v91, v228
	v_mul_f32_dpp v228, v92, v248 quad_perm:[1,0,3,2] row_mask:0xf bank_mask:0xf
	v_mul_f32_e32 v92, v92, v248
	v_cvt_pk_bf16_f32 v92, v92, v228
	v_mul_f32_dpp v228, v93, v249 quad_perm:[1,0,3,2] row_mask:0xf bank_mask:0xf
	v_mul_f32_e32 v93, v93, v249
	v_cvt_pk_bf16_f32 v93, v93, v228
	v_mul_f32_dpp v228, v94, v250 quad_perm:[1,0,3,2] row_mask:0xf bank_mask:0xf
	v_mul_f32_e32 v94, v94, v250
	v_cvt_pk_bf16_f32 v94, v94, v228
	v_mul_f32_dpp v228, v95, v251 quad_perm:[1,0,3,2] row_mask:0xf bank_mask:0xf
	v_mul_f32_e32 v95, v95, v251
	v_cvt_pk_bf16_f32 v95, v95, v228
	v_mul_f32_dpp v228, v98, v236 quad_perm:[1,0,3,2] row_mask:0xf bank_mask:0xf
	v_mul_f32_e32 v98, v98, v236
	v_cvt_pk_bf16_f32 v98, v98, v228
	v_mul_f32_dpp v228, v99, v237 quad_perm:[1,0,3,2] row_mask:0xf bank_mask:0xf
	v_mul_f32_e32 v99, v99, v237
	v_cvt_pk_bf16_f32 v99, v99, v228
	v_mul_f32_dpp v228, v100, v238 quad_perm:[1,0,3,2] row_mask:0xf bank_mask:0xf
	v_mul_f32_e32 v100, v100, v238
	v_cvt_pk_bf16_f32 v100, v100, v228
	v_mul_f32_dpp v228, v101, v239 quad_perm:[1,0,3,2] row_mask:0xf bank_mask:0xf
	v_mul_f32_e32 v101, v101, v239
	v_cvt_pk_bf16_f32 v101, v101, v228
	v_mul_f32_dpp v228, v102, v240 quad_perm:[1,0,3,2] row_mask:0xf bank_mask:0xf
	v_mul_f32_e32 v102, v102, v240
	v_cvt_pk_bf16_f32 v102, v102, v228
	v_mul_f32_dpp v228, v103, v241 quad_perm:[1,0,3,2] row_mask:0xf bank_mask:0xf
	v_mul_f32_e32 v103, v103, v241
	v_cvt_pk_bf16_f32 v103, v103, v228
	v_mul_f32_dpp v228, v104, v242 quad_perm:[1,0,3,2] row_mask:0xf bank_mask:0xf
	v_mul_f32_e32 v104, v104, v242
	v_cvt_pk_bf16_f32 v104, v104, v228
	v_mul_f32_dpp v228, v105, v243 quad_perm:[1,0,3,2] row_mask:0xf bank_mask:0xf
	v_mul_f32_e32 v105, v105, v243
	v_cvt_pk_bf16_f32 v105, v105, v228
	v_mul_f32_dpp v228, v106, v244 quad_perm:[1,0,3,2] row_mask:0xf bank_mask:0xf
	v_mul_f32_e32 v106, v106, v244
	v_cvt_pk_bf16_f32 v106, v106, v228
	v_mul_f32_dpp v228, v107, v245 quad_perm:[1,0,3,2] row_mask:0xf bank_mask:0xf
	v_mul_f32_e32 v107, v107, v245
	v_cvt_pk_bf16_f32 v107, v107, v228
	v_mul_f32_dpp v228, v108, v246 quad_perm:[1,0,3,2] row_mask:0xf bank_mask:0xf
	v_mul_f32_e32 v108, v108, v246
	v_cvt_pk_bf16_f32 v108, v108, v228
	v_mul_f32_dpp v228, v109, v247 quad_perm:[1,0,3,2] row_mask:0xf bank_mask:0xf
	v_mul_f32_e32 v109, v109, v247
	v_cvt_pk_bf16_f32 v109, v109, v228
	v_mul_f32_dpp v228, v110, v248 quad_perm:[1,0,3,2] row_mask:0xf bank_mask:0xf
	v_mul_f32_e32 v110, v110, v248
	v_cvt_pk_bf16_f32 v110, v110, v228
	v_mul_f32_dpp v228, v111, v249 quad_perm:[1,0,3,2] row_mask:0xf bank_mask:0xf
	v_mul_f32_e32 v111, v111, v249
	v_cvt_pk_bf16_f32 v111, v111, v228
	v_mul_f32_dpp v228, v112, v250 quad_perm:[1,0,3,2] row_mask:0xf bank_mask:0xf
	v_mul_f32_e32 v112, v112, v250
	v_cvt_pk_bf16_f32 v112, v112, v228
	v_mul_f32_dpp v228, v113, v251 quad_perm:[1,0,3,2] row_mask:0xf bank_mask:0xf
	v_mul_f32_e32 v113, v113, v251
	v_cvt_pk_bf16_f32 v113, v113, v228
	v_mul_f32_dpp v228, v114, v236 quad_perm:[1,0,3,2] row_mask:0xf bank_mask:0xf
	v_mul_f32_e32 v114, v114, v236
	v_cvt_pk_bf16_f32 v114, v114, v228
	v_mul_f32_dpp v228, v115, v237 quad_perm:[1,0,3,2] row_mask:0xf bank_mask:0xf
	v_mul_f32_e32 v115, v115, v237
	v_cvt_pk_bf16_f32 v115, v115, v228
	v_mul_f32_dpp v228, v116, v238 quad_perm:[1,0,3,2] row_mask:0xf bank_mask:0xf
	v_mul_f32_e32 v116, v116, v238
	v_cvt_pk_bf16_f32 v116, v116, v228
	v_mul_f32_dpp v228, v117, v239 quad_perm:[1,0,3,2] row_mask:0xf bank_mask:0xf
	v_mul_f32_e32 v117, v117, v239
	v_cvt_pk_bf16_f32 v117, v117, v228
	v_mul_f32_dpp v228, v118, v240 quad_perm:[1,0,3,2] row_mask:0xf bank_mask:0xf
	v_mul_f32_e32 v118, v118, v240
	v_cvt_pk_bf16_f32 v118, v118, v228
	v_mul_f32_dpp v228, v119, v241 quad_perm:[1,0,3,2] row_mask:0xf bank_mask:0xf
	v_mul_f32_e32 v119, v119, v241
	v_cvt_pk_bf16_f32 v119, v119, v228
	v_mul_f32_dpp v228, v120, v242 quad_perm:[1,0,3,2] row_mask:0xf bank_mask:0xf
	v_mul_f32_e32 v120, v120, v242
	v_cvt_pk_bf16_f32 v120, v120, v228
	v_mul_f32_dpp v228, v121, v243 quad_perm:[1,0,3,2] row_mask:0xf bank_mask:0xf
	v_mul_f32_e32 v121, v121, v243
	v_cvt_pk_bf16_f32 v121, v121, v228
	v_mul_f32_dpp v228, v122, v244 quad_perm:[1,0,3,2] row_mask:0xf bank_mask:0xf
	v_mul_f32_e32 v122, v122, v244
	v_cvt_pk_bf16_f32 v122, v122, v228
	v_mul_f32_dpp v228, v123, v245 quad_perm:[1,0,3,2] row_mask:0xf bank_mask:0xf
	v_mul_f32_e32 v123, v123, v245
	v_cvt_pk_bf16_f32 v123, v123, v228
	v_mul_f32_dpp v228, v124, v246 quad_perm:[1,0,3,2] row_mask:0xf bank_mask:0xf
	v_mul_f32_e32 v124, v124, v246
	v_cvt_pk_bf16_f32 v124, v124, v228
	v_mul_f32_dpp v228, v125, v247 quad_perm:[1,0,3,2] row_mask:0xf bank_mask:0xf
	v_mul_f32_e32 v125, v125, v247
	v_cvt_pk_bf16_f32 v125, v125, v228
	v_mul_f32_dpp v228, v126, v248 quad_perm:[1,0,3,2] row_mask:0xf bank_mask:0xf
	v_mul_f32_e32 v126, v126, v248
	v_cvt_pk_bf16_f32 v126, v126, v228
	v_mul_f32_dpp v228, v127, v249 quad_perm:[1,0,3,2] row_mask:0xf bank_mask:0xf
	v_mul_f32_e32 v127, v127, v249
	v_cvt_pk_bf16_f32 v127, v127, v228
	v_mul_f32_dpp v228, v128, v250 quad_perm:[1,0,3,2] row_mask:0xf bank_mask:0xf
	v_mul_f32_e32 v128, v128, v250
	v_cvt_pk_bf16_f32 v128, v128, v228
	v_mul_f32_dpp v228, v129, v251 quad_perm:[1,0,3,2] row_mask:0xf bank_mask:0xf
	v_mul_f32_e32 v129, v129, v251
	v_cvt_pk_bf16_f32 v129, v129, v228
	s_barrier
	s_lshl_b32 s21, s15, 13
	v_lshlrev_b32_e32 v233, 10, v229
	v_lshl_add_u32 v233, v231, 1, v233
	v_add_u32_e32 v233, s21, v233
	v_mbcnt_lo_u32_b32 v234, -1, 0
	v_mbcnt_hi_u32_b32 v234, -1, v234
	v_lshlrev_b32_e32 v234, 4, v234
	v_add_u32_e32 v230, s21, v234
	v_add_u32_e32 v232, 0x1000, v230
	v_add_u32_e32 v234, s21, v234
	s_mov_b64 s[48:49], exec
	s_mov_b32 s50, 0x55555555
	s_mov_b32 s51, 0x55555555
	s_mov_b64 exec, s[50:51]
	ds_write_b32 v233, v0 offset:0
	ds_write_b32 v233, v1 offset:256
	ds_write_b32 v233, v2 offset:512
	ds_write_b32 v233, v3 offset:768
	ds_write_b32 v233, v4 offset:2048
	ds_write_b32 v233, v5 offset:2304
	ds_write_b32 v233, v6 offset:2560
	ds_write_b32 v233, v7 offset:2816
	ds_write_b32 v233, v8 offset:4096
	ds_write_b32 v233, v9 offset:4352
	ds_write_b32 v233, v10 offset:4608
	ds_write_b32 v233, v11 offset:4864
	ds_write_b32 v233, v12 offset:6144
	ds_write_b32 v233, v13 offset:6400
	ds_write_b32 v233, v14 offset:6656
	ds_write_b32 v233, v15 offset:6912
	ds_write_b32 v233, v16 offset:64
	ds_write_b32 v233, v17 offset:320
	ds_write_b32 v233, v18 offset:576
	ds_write_b32 v233, v19 offset:832
	ds_write_b32 v233, v20 offset:2112
	ds_write_b32 v233, v21 offset:2368
	ds_write_b32 v233, v22 offset:2624
	ds_write_b32 v233, v23 offset:2880
	ds_write_b32 v233, v24 offset:4160
	ds_write_b32 v233, v25 offset:4416
	ds_write_b32 v233, v26 offset:4672
	ds_write_b32 v233, v27 offset:4928
	ds_write_b32 v233, v28 offset:6208
	ds_write_b32 v233, v29 offset:6464
	ds_write_b32 v233, v30 offset:6720
	ds_write_b32 v233, v31 offset:6976
	ds_write_b32 v233, v32 offset:128
	ds_write_b32 v233, v33 offset:384
	ds_write_b32 v233, v34 offset:640
	ds_write_b32 v233, v35 offset:896
	ds_write_b32 v233, v36 offset:2176
	ds_write_b32 v233, v37 offset:2432
	ds_write_b32 v233, v38 offset:2688
	ds_write_b32 v233, v39 offset:2944
	ds_write_b32 v233, v40 offset:4224
	ds_write_b32 v233, v41 offset:4480
	ds_write_b32 v233, v42 offset:4736
	ds_write_b32 v233, v43 offset:4992
	ds_write_b32 v233, v44 offset:6272
	ds_write_b32 v233, v45 offset:6528
	ds_write_b32 v233, v46 offset:6784
	ds_write_b32 v233, v47 offset:7040
	ds_write_b32 v233, v48 offset:192
	ds_write_b32 v233, v49 offset:448
	ds_write_b32 v233, v50 offset:704
	ds_write_b32 v233, v51 offset:960
	ds_write_b32 v233, v52 offset:2240
	ds_write_b32 v233, v53 offset:2496
	ds_write_b32 v233, v54 offset:2752
	ds_write_b32 v233, v55 offset:3008
	ds_write_b32 v233, v56 offset:4288
	ds_write_b32 v233, v57 offset:4544
	ds_write_b32 v233, v58 offset:4800
	ds_write_b32 v233, v59 offset:5056
	ds_write_b32 v233, v60 offset:6336
	ds_write_b32 v233, v61 offset:6592
	ds_write_b32 v233, v62 offset:6848
	ds_write_b32 v233, v63 offset:7104
	s_mov_b64 exec, s[48:49]
	s_waitcnt lgkmcnt(0)
	ds_read_b128 v[236:239], v234 offset:0
	ds_read_b128 v[240:243], v234 offset:1024
	ds_read_b128 v[244:247], v234 offset:2048
	ds_read_b128 v[248:251], v234 offset:3072
	ds_read_b128 v[194:197], v234 offset:4096
	ds_read_b128 v[198:201], v234 offset:5120
	ds_read_b128 v[212:215], v234 offset:6144
	ds_read_b128 v[216:219], v234 offset:7168
	s_waitcnt lgkmcnt(0)
	global_store_dwordx4 v230, v[236:239], s[42:43] offset:0
	global_store_dwordx4 v230, v[240:243], s[42:43] offset:1024
	global_store_dwordx4 v230, v[244:247], s[42:43] offset:2048
	global_store_dwordx4 v230, v[248:251], s[42:43] offset:3072
	global_store_dwordx4 v232, v[194:197], s[42:43] offset:0
	global_store_dwordx4 v232, v[198:201], s[42:43] offset:1024
	global_store_dwordx4 v232, v[212:215], s[42:43] offset:2048
	global_store_dwordx4 v232, v[216:219], s[42:43] offset:3072
	s_nop 1
	s_mov_b64 exec, s[50:51]
	ds_write_b32 v233, v64 offset:0
	ds_write_b32 v233, v65 offset:256
	ds_write_b32 v233, v66 offset:512
	ds_write_b32 v233, v67 offset:768
	ds_write_b32 v233, v68 offset:2048
	ds_write_b32 v233, v69 offset:2304
	ds_write_b32 v233, v70 offset:2560
	ds_write_b32 v233, v71 offset:2816
	ds_write_b32 v233, v72 offset:4096
	ds_write_b32 v233, v73 offset:4352
	ds_write_b32 v233, v74 offset:4608
	ds_write_b32 v233, v75 offset:4864
	ds_write_b32 v233, v76 offset:6144
	ds_write_b32 v233, v77 offset:6400
	ds_write_b32 v233, v78 offset:6656
	ds_write_b32 v233, v79 offset:6912
	ds_write_b32 v233, v80 offset:64
	ds_write_b32 v233, v81 offset:320
	ds_write_b32 v233, v82 offset:576
	ds_write_b32 v233, v83 offset:832
	ds_write_b32 v233, v84 offset:2112
	ds_write_b32 v233, v85 offset:2368
	ds_write_b32 v233, v86 offset:2624
	ds_write_b32 v233, v87 offset:2880
	ds_write_b32 v233, v88 offset:4160
	ds_write_b32 v233, v89 offset:4416
	ds_write_b32 v233, v90 offset:4672
	ds_write_b32 v233, v91 offset:4928
	ds_write_b32 v233, v92 offset:6208
	ds_write_b32 v233, v93 offset:6464
	ds_write_b32 v233, v94 offset:6720
	ds_write_b32 v233, v95 offset:6976
	ds_write_b32 v233, v98 offset:128
	ds_write_b32 v233, v99 offset:384
	ds_write_b32 v233, v100 offset:640
	ds_write_b32 v233, v101 offset:896
	ds_write_b32 v233, v102 offset:2176
	ds_write_b32 v233, v103 offset:2432
	ds_write_b32 v233, v104 offset:2688
	ds_write_b32 v233, v105 offset:2944
	ds_write_b32 v233, v106 offset:4224
	ds_write_b32 v233, v107 offset:4480
	ds_write_b32 v233, v108 offset:4736
	ds_write_b32 v233, v109 offset:4992
	ds_write_b32 v233, v110 offset:6272
	ds_write_b32 v233, v111 offset:6528
	ds_write_b32 v233, v112 offset:6784
	ds_write_b32 v233, v113 offset:7040
	ds_write_b32 v233, v114 offset:192
	ds_write_b32 v233, v115 offset:448
	ds_write_b32 v233, v116 offset:704
	ds_write_b32 v233, v117 offset:960
	ds_write_b32 v233, v118 offset:2240
	ds_write_b32 v233, v119 offset:2496
	ds_write_b32 v233, v120 offset:2752
	ds_write_b32 v233, v121 offset:3008
	ds_write_b32 v233, v122 offset:4288
	ds_write_b32 v233, v123 offset:4544
	ds_write_b32 v233, v124 offset:4800
	ds_write_b32 v233, v125 offset:5056
	ds_write_b32 v233, v126 offset:6336
	ds_write_b32 v233, v127 offset:6592
	ds_write_b32 v233, v128 offset:6848
	ds_write_b32 v233, v129 offset:7104
	s_mov_b64 exec, s[48:49]
	s_waitcnt lgkmcnt(0)
	ds_read_b128 v[236:239], v234 offset:0
	ds_read_b128 v[240:243], v234 offset:1024
	ds_read_b128 v[244:247], v234 offset:2048
	ds_read_b128 v[248:251], v234 offset:3072
	ds_read_b128 v[194:197], v234 offset:4096
	ds_read_b128 v[198:201], v234 offset:5120
	ds_read_b128 v[212:215], v234 offset:6144
	ds_read_b128 v[216:219], v234 offset:7168
	s_waitcnt lgkmcnt(0)
	global_store_dwordx4 v230, v[236:239], s[44:45] offset:0
	global_store_dwordx4 v230, v[240:243], s[44:45] offset:1024
	global_store_dwordx4 v230, v[244:247], s[44:45] offset:2048
	global_store_dwordx4 v230, v[248:251], s[44:45] offset:3072
	global_store_dwordx4 v232, v[194:197], s[44:45] offset:0
	global_store_dwordx4 v232, v[198:201], s[44:45] offset:1024
	global_store_dwordx4 v232, v[212:215], s[44:45] offset:2048
	global_store_dwordx4 v232, v[216:219], s[44:45] offset:3072
	s_nop 1
	s_barrier
	s_branch .Lfa_epi_done
